# baseline (speedup 1.0000x reference)
.LBB0_37:
	s_or_b64 exec, exec, s[14:15]
	v_readfirstlane_b32 s94, v0
	s_lshr_b32 s94, s94, 6
	s_cmp_lg_u32 s94, 1
	s_cbranch_scc1 .Llpt_done
	s_add_i32 s95, s33, 1
	s_ashr_i32 s95, s95, 1
	v_add_u32_e32 v100, 16, v3
	v_add_u32_e32 v101, 0x50, v3
	v_lshlrev_b32_e32 v102, 3, v100
	v_lshlrev_b32_e32 v103, 3, v101
	v_add_u32_e32 v102, 0x1dd00, v102
	v_add_u32_e32 v103, 0x1dd00, v103
	ds_read_b64 v[104:105], v102
	ds_read_b64 v[106:107], v103
	v_mov_b32_e32 v110, 0x26d50
	s_waitcnt lgkmcnt(0)
	v_add_u32_e32 v104, v104, v105
	v_add_u32_e32 v106, v106, v107
	v_add_u32_e32 v104, 15, v104
	v_add_u32_e32 v106, 15, v106
	v_lshrrev_b32_e32 v104, 4, v104
	v_lshrrev_b32_e32 v106, 4, v106
	v_max_u32_e32 v104, 1, v104
	v_max_u32_e32 v106, 1, v106
	v_min_u32_e32 v104, 7, v104
	v_min_u32_e32 v106, 7, v106
	v_cmp_gt_i32_e32 vcc, s95, v100
	s_nop 1
	v_cndmask_b32_e32 v104, 0, v104, vcc
	v_cmp_gt_i32_e32 vcc, s95, v101
	s_nop 1
	v_cndmask_b32_e32 v106, 0, v106, vcc
	s_mov_b32 s94, 16
	v_cmp_eq_u32_e64 s[34:35], 7, v104
	v_cmp_eq_u32_e64 s[36:37], 7, v106
	s_bcnt1_i32_b64 s73, s[34:35]
	s_nop 0
	v_mbcnt_lo_u32_b32 v108, s34, 0
	v_mbcnt_hi_u32_b32 v108, s35, v108
	v_add_u32_e32 v108, s94, v108
	s_add_i32 s94, s94, s73
	v_mbcnt_lo_u32_b32 v109, s36, 0
	v_mbcnt_hi_u32_b32 v109, s37, v109
	v_add_u32_e32 v109, s94, v109
	s_bcnt1_i32_b64 s73, s[36:37]
	s_add_i32 s94, s94, s73
	v_lshl_add_u32 v108, v108, 2, v110
	v_lshl_add_u32 v109, v109, 2, v110
	s_mov_b64 exec, s[34:35]
	ds_write_b32 v108, v100
	s_mov_b64 exec, s[36:37]
	ds_write_b32 v109, v101
	s_mov_b64 exec, -1
	v_cmp_eq_u32_e64 s[34:35], 6, v104
	v_cmp_eq_u32_e64 s[36:37], 6, v106
	s_bcnt1_i32_b64 s73, s[34:35]
	s_nop 0
	v_mbcnt_lo_u32_b32 v108, s34, 0
	v_mbcnt_hi_u32_b32 v108, s35, v108
	v_add_u32_e32 v108, s94, v108
	s_add_i32 s94, s94, s73
	v_mbcnt_lo_u32_b32 v109, s36, 0
	v_mbcnt_hi_u32_b32 v109, s37, v109
	v_add_u32_e32 v109, s94, v109
	s_bcnt1_i32_b64 s73, s[36:37]
	s_add_i32 s94, s94, s73
	v_lshl_add_u32 v108, v108, 2, v110
	v_lshl_add_u32 v109, v109, 2, v110
	s_mov_b64 exec, s[34:35]
	ds_write_b32 v108, v100
	s_mov_b64 exec, s[36:37]
	ds_write_b32 v109, v101
	s_mov_b64 exec, -1
	v_cmp_eq_u32_e64 s[34:35], 5, v104
	v_cmp_eq_u32_e64 s[36:37], 5, v106
	s_bcnt1_i32_b64 s73, s[34:35]
	s_nop 0
	v_mbcnt_lo_u32_b32 v108, s34, 0
	v_mbcnt_hi_u32_b32 v108, s35, v108
	v_add_u32_e32 v108, s94, v108
	s_add_i32 s94, s94, s73
	v_mbcnt_lo_u32_b32 v109, s36, 0
	v_mbcnt_hi_u32_b32 v109, s37, v109
	v_add_u32_e32 v109, s94, v109
	s_bcnt1_i32_b64 s73, s[36:37]
	s_add_i32 s94, s94, s73
	v_lshl_add_u32 v108, v108, 2, v110
	v_lshl_add_u32 v109, v109, 2, v110
	s_mov_b64 exec, s[34:35]
	ds_write_b32 v108, v100
	s_mov_b64 exec, s[36:37]
	ds_write_b32 v109, v101
	s_mov_b64 exec, -1
	v_cmp_eq_u32_e64 s[34:35], 4, v104
	v_cmp_eq_u32_e64 s[36:37], 4, v106
	s_bcnt1_i32_b64 s73, s[34:35]
	s_nop 0
	v_mbcnt_lo_u32_b32 v108, s34, 0
	v_mbcnt_hi_u32_b32 v108, s35, v108
	v_add_u32_e32 v108, s94, v108
	s_add_i32 s94, s94, s73
	v_mbcnt_lo_u32_b32 v109, s36, 0
	v_mbcnt_hi_u32_b32 v109, s37, v109
	v_add_u32_e32 v109, s94, v109
	s_bcnt1_i32_b64 s73, s[36:37]
	s_add_i32 s94, s94, s73
	v_lshl_add_u32 v108, v108, 2, v110
	v_lshl_add_u32 v109, v109, 2, v110
	s_mov_b64 exec, s[34:35]
	ds_write_b32 v108, v100
	s_mov_b64 exec, s[36:37]
	ds_write_b32 v109, v101
	s_mov_b64 exec, -1
	v_cmp_eq_u32_e64 s[34:35], 3, v104
	v_cmp_eq_u32_e64 s[36:37], 3, v106
	s_bcnt1_i32_b64 s73, s[34:35]
	s_nop 0
	v_mbcnt_lo_u32_b32 v108, s34, 0
	v_mbcnt_hi_u32_b32 v108, s35, v108
	v_add_u32_e32 v108, s94, v108
	s_add_i32 s94, s94, s73
	v_mbcnt_lo_u32_b32 v109, s36, 0
	v_mbcnt_hi_u32_b32 v109, s37, v109
	v_add_u32_e32 v109, s94, v109
	s_bcnt1_i32_b64 s73, s[36:37]
	s_add_i32 s94, s94, s73
	v_lshl_add_u32 v108, v108, 2, v110
	v_lshl_add_u32 v109, v109, 2, v110
	s_mov_b64 exec, s[34:35]
	ds_write_b32 v108, v100
	s_mov_b64 exec, s[36:37]
	ds_write_b32 v109, v101
	s_mov_b64 exec, -1
	v_cmp_eq_u32_e64 s[34:35], 2, v104
	v_cmp_eq_u32_e64 s[36:37], 2, v106
	s_bcnt1_i32_b64 s73, s[34:35]
	s_nop 0
	v_mbcnt_lo_u32_b32 v108, s34, 0
	v_mbcnt_hi_u32_b32 v108, s35, v108
	v_add_u32_e32 v108, s94, v108
	s_add_i32 s94, s94, s73
	v_mbcnt_lo_u32_b32 v109, s36, 0
	v_mbcnt_hi_u32_b32 v109, s37, v109
	v_add_u32_e32 v109, s94, v109
	s_bcnt1_i32_b64 s73, s[36:37]
	s_add_i32 s94, s94, s73
	v_lshl_add_u32 v108, v108, 2, v110
	v_lshl_add_u32 v109, v109, 2, v110
	s_mov_b64 exec, s[34:35]
	ds_write_b32 v108, v100
	s_mov_b64 exec, s[36:37]
	ds_write_b32 v109, v101
	s_mov_b64 exec, -1
	v_cmp_eq_u32_e64 s[34:35], 1, v104
	v_cmp_eq_u32_e64 s[36:37], 1, v106
	s_bcnt1_i32_b64 s73, s[34:35]
	s_nop 0
	v_mbcnt_lo_u32_b32 v108, s34, 0
	v_mbcnt_hi_u32_b32 v108, s35, v108
	v_add_u32_e32 v108, s94, v108
	s_add_i32 s94, s94, s73
	v_mbcnt_lo_u32_b32 v109, s36, 0
	v_mbcnt_hi_u32_b32 v109, s37, v109
	v_add_u32_e32 v109, s94, v109
	s_bcnt1_i32_b64 s73, s[36:37]
	s_add_i32 s94, s94, s73
	v_lshl_add_u32 v108, v108, 2, v110
	v_lshl_add_u32 v109, v109, 2, v110
	s_mov_b64 exec, s[34:35]
	ds_write_b32 v108, v100
	s_mov_b64 exec, s[36:37]
	ds_write_b32 v109, v101
	s_mov_b64 exec, -1
.Llpt_done:
	s_load_dwordx4 s[52:55], s[0:1], 0x40
	s_load_dwordx2 s[14:15], s[0:1], 0x0
	s_load_dwordx2 s[22:23], s[0:1], 0x30
	s_mov_b64 vcc, s[4:5]
	v_mov_b32_e32 v4, 0
	v_cndmask_b32_e32 v7, 0, v20, vcc
	s_waitcnt vmcnt(0)
	v_mov_b32_e32 v6, 0
	s_waitcnt lgkmcnt(0)
	s_barrier
	v_cmp_gt_u32_e32 vcc, 0x80, v0
	s_and_saveexec_b64 s[64:65], vcc
	s_cbranch_execz .Lbv_ld_skip
	v_lshlrev_b32_e32 v118, 2, v0
	global_load_dword v119, v118, s[22:23]

.LBB0_71:
	s_or_b64 exec, exec, s[0:1]
	s_add_i32 s0, s33, 1
	s_ashr_i32 s68, s0, 1
	v_readfirstlane_b32 s18, v4
	s_cmp_ge_i32 s18, s68
	s_cbranch_scc1 .Llpt_map1
	s_lshl_b32 s94, s18, 2
	s_add_i32 s94, s94, 0x26d50
	v_mov_b32_e32 v117, s94
	ds_read_b32 v117, v117
	s_waitcnt lgkmcnt(0)
	v_readfirstlane_b32 s18, v117
.Llpt_map1:
	v_cmp_gt_i32_e32 vcc, s68, v80
	v_mov_b32_e32 v4, 0
	v_mov_b32_e32 v99, 4
	v_mov_b32_e32 v5, 4
	s_and_saveexec_b64 s[4:5], vcc
	s_cbranch_execz .LBB0_75
	v_mov_b32_e32 v4, 0x26500
	v_lshl_add_u32 v4, v12, 3, v4
	ds_read_b64 v[4:5], v4
	v_cmp_gt_i32_e64 s[0:1], s33, v11
	s_waitcnt lgkmcnt(0)
	v_readfirstlane_b32 s8, v4
	v_readfirstlane_b32 s9, v5
	v_mov_b32_e32 v4, 0
	s_and_saveexec_b64 s[6:7], s[0:1]
	s_cbranch_execz .LBB0_74
	v_mov_b32_e32 v4, 0x26504
	v_lshl_add_u32 v4, v10, 3, v4
	ds_read_b32 v4, v4
	s_waitcnt lgkmcnt(0)
	v_readfirstlane_b32 s0, v4
	s_nop 1
	v_mov_b32_e32 v4, s0

.LBB0_81:
	s_or_b64 exec, exec, s[8:9]
	v_readfirstlane_b32 s0, v7
	s_cmp_ge_i32 s0, s68
	s_cbranch_scc1 .Llpt_map2
	s_lshl_b32 s94, s0, 2
	s_add_i32 s94, s94, 0x26d50
	v_mov_b32_e32 v117, s94
	ds_read_b32 v117, v117
	s_waitcnt lgkmcnt(0)
	v_readfirstlane_b32 s0, v117
.Llpt_map2:
	s_cmp_ge_i32 s18, s68
	v_mov_b32_e32 v85, v4
	v_mov_b32_e32 v81, v5
	v_mov_b32_e32 v83, v99
	s_cbranch_scc1 .LBB0_85
	s_lshl_b32 s1, s18, 1
	s_min_i32 s8, s1, s67
	s_lshl_b32 s8, s8, 3
	s_add_i32 s8, s8, 0x26500
	v_mov_b32_e32 v7, s8
	ds_read_b64 v[8:9], v7
	s_or_b32 s8, s1, 1
	s_cmp_ge_i32 s8, s33
	s_mov_b32 s10, 0
	s_waitcnt lgkmcnt(0)
	v_readfirstlane_b32 s8, v8
	v_readfirstlane_b32 s9, v9
	s_cbranch_scc1 .LBB0_84
	s_lshl_b32 s1, s1, 3
	s_add_i32 s1, s1, 0x2650c
	v_mov_b32_e32 v7, s1
	ds_read_b32 v7, v7
	s_waitcnt lgkmcnt(0)
	v_readfirstlane_b32 s10, v7

.Lattn_map:
	s_cmp_ge_i32 s101, s68
	s_cbranch_scc1 .Lattn_map_done
	s_lshl_b32 s94, s101, 2
	s_add_i32 s94, s94, 0x26d50
	v_mov_b32_e32 v2, s94
	ds_read_b32 v2, v2
	s_waitcnt lgkmcnt(0)
	v_readfirstlane_b32 s101, v2
.Lattn_map_done:
	s_branch .LBB0_95
.LBB0_117:
	s_branch .LBB0_99

	.amdhsa_kernel _Z7k_attn3PKDF16_S0_PKiS2_PiPKDv8_DF16_PKfS6_S8_Pf
		.amdhsa_group_segment_fixed_size 159568
		.amdhsa_private_segment_fixed_size 0
		.amdhsa_kernarg_size 80
		.amdhsa_user_sgpr_count 2
		.amdhsa_user_sgpr_dispatch_ptr 0
		.amdhsa_user_sgpr_queue_ptr 0
		.amdhsa_user_sgpr_kernarg_segment_ptr 1
		.amdhsa_user_sgpr_dispatch_id 0
		.amdhsa_user_sgpr_kernarg_preload_length 0
		.amdhsa_user_sgpr_kernarg_preload_offset 0
		.amdhsa_user_sgpr_private_segment_size 0
		.amdhsa_uses_dynamic_stack 0
		.amdhsa_enable_private_segment 0
		.amdhsa_system_sgpr_workgroup_id_x 1
		.amdhsa_system_sgpr_workgroup_id_y 0
		.amdhsa_system_sgpr_workgroup_id_z 0
		.amdhsa_system_sgpr_workgroup_info 0
		.amdhsa_system_vgpr_workitem_id 0
		.amdhsa_next_free_vgpr 128
		.amdhsa_next_free_sgpr 102
		.amdhsa_accum_offset 128
		.amdhsa_reserve_vcc 1
		.amdhsa_float_round_mode_32 0
		.amdhsa_float_round_mode_16_64 0
		.amdhsa_float_denorm_mode_32 3
		.amdhsa_float_denorm_mode_16_64 3
		.amdhsa_dx10_clamp 1
		.amdhsa_ieee_mode 1
		.amdhsa_fp16_overflow 0
		.amdhsa_tg_split 0
		.amdhsa_exception_fp_ieee_invalid_op 0
		.amdhsa_exception_fp_denorm_src 0
		.amdhsa_exception_fp_ieee_div_zero 0
		.amdhsa_exception_fp_ieee_overflow 0
		.amdhsa_exception_fp_ieee_underflow 0
		.amdhsa_exception_fp_ieee_inexact 0
		.amdhsa_exception_int_div_zero 0
	.end_amdhsa_kernel

amdhsa.kernels:
  - .agpr_count:     0
    .args:
      - .actual_access:  read_only
        .address_space:  global
        .offset:         0
        .size:           8
        .value_kind:     global_buffer
      - .actual_access:  read_only
        .address_space:  global
        .offset:         8
        .size:           8
        .value_kind:     global_buffer
      - .actual_access:  read_only
        .address_space:  global
        .offset:         16
        .size:           8
        .value_kind:     global_buffer
      - .actual_access:  read_only
        .address_space:  global
        .offset:         24
        .size:           8
        .value_kind:     global_buffer
      - .address_space:  global
        .offset:         32
        .size:           8
        .value_kind:     global_buffer
      - .actual_access:  read_only
        .address_space:  global
        .offset:         40
        .size:           8
        .value_kind:     global_buffer
      - .actual_access:  read_only
        .address_space:  global
        .offset:         48
        .size:           8
        .value_kind:     global_buffer
      - .actual_access:  read_only
        .address_space:  global
        .offset:         56
        .size:           8
        .value_kind:     global_buffer
      - .actual_access:  read_only
        .address_space:  global
        .offset:         64
        .size:           8
        .value_kind:     global_buffer
      - .actual_access:  write_only
        .address_space:  global
        .offset:         72
        .size:           8
        .value_kind:     global_buffer
    .group_segment_fixed_size: 159568
    .kernarg_segment_align: 8
    .kernarg_segment_size: 80
    .language:       OpenCL C
    .language_version:
      - 2
      - 0
    .max_flat_workgroup_size: 1024
    .name:           _Z7k_attn3PKDF16_S0_PKiS2_PiPKDv8_DF16_PKfS6_S8_Pf
    .private_segment_fixed_size: 0
    .sgpr_count:     79
    .sgpr_spill_count: 0
    .symbol:         _Z7k_attn3PKDF16_S0_PKiS2_PiPKDv8_DF16_PKfS6_S8_Pf.kd
    .uniform_work_group_size: 1
    .uses_dynamic_stack: false
    .vgpr_count:     128
    .vgpr_spill_count: 0
    .wavefront_size: 64
  - .agpr_count:     0
    .args:
      - .actual_access:  read_only
        .address_space:  global
        .offset:         0
        .size:           8
        .value_kind:     global_buffer
      - .actual_access:  write_only
        .address_space:  global
        .offset:         8
        .size:           8
        .value_kind:     global_buffer
      - .actual_access:  read_only
        .address_space:  global
        .offset:         16
        .size:           8
        .value_kind:     global_buffer
      - .actual_access:  read_only
        .address_space:  global
        .offset:         24
        .size:           8
        .value_kind:     global_buffer
      - .actual_access:  read_only
        .address_space:  global
        .offset:         32
        .size:           8
        .value_kind:     global_buffer
      - .actual_access:  read_only
        .address_space:  global
        .offset:         40
        .size:           8
        .value_kind:     global_buffer
      - .actual_access:  read_only
        .address_space:  global
        .offset:         48
        .size:           8
        .value_kind:     global_buffer
      - .actual_access:  read_only
        .address_space:  global
        .offset:         56
        .size:           8
        .value_kind:     global_buffer
      - .actual_access:  read_only
        .address_space:  global
        .offset:         64
        .size:           8
        .value_kind:     global_buffer
      - .actual_access:  write_only
        .address_space:  global
        .offset:         72
        .size:           8
        .value_kind:     global_buffer
      - .actual_access:  write_only
        .address_space:  global
        .offset:         80
        .size:           8
        .value_kind:     global_buffer
      - .actual_access:  write_only
        .address_space:  global
        .offset:         88
        .size:           8
        .value_kind:     global_buffer
      - .actual_access:  write_only
        .address_space:  global
        .offset:         96
        .size:           8
        .value_kind:     global_buffer
    .group_segment_fixed_size: 1024
    .kernarg_segment_align: 8
    .kernarg_segment_size: 104
    .language:       OpenCL C
    .language_version:
      - 2
      - 0
    .max_flat_workgroup_size: 512
    .name:           _Z4k_l1PK15HIP_vector_typeIiLj4EEPiPKfS5_S5_S5_S5_S5_S5_PDF16_PfS6_S6_
    .private_segment_fixed_size: 0
    .sgpr_count:     22
    .sgpr_spill_count: 0
    .symbol:         _Z4k_l1PK15HIP_vector_typeIiLj4EEPiPKfS5_S5_S5_S5_S5_S5_PDF16_PfS6_S6_.kd
    .uniform_work_group_size: 1
    .uses_dynamic_stack: false
    .vgpr_count:     24
    .vgpr_spill_count: 0
    .wavefront_size: 64
  - .agpr_count:     0
    .args:
      - .actual_access:  read_only
        .address_space:  global
        .offset:         0
        .size:           8
        .value_kind:     global_buffer
      - .actual_access:  read_only
        .address_space:  global
        .offset:         8
        .size:           8
        .value_kind:     global_buffer
      - .actual_access:  read_only
        .address_space:  global
        .offset:         16
        .size:           8
        .value_kind:     global_buffer
      - .actual_access:  write_only
        .address_space:  global
        .offset:         24
        .size:           8
        .value_kind:     global_buffer
      - .actual_access:  write_only
        .address_space:  global
        .offset:         32
        .size:           8
        .value_kind:     global_buffer
      - .actual_access:  read_only
        .address_space:  global
        .offset:         40
        .size:           8
        .value_kind:     global_buffer
      - .actual_access:  read_only
        .address_space:  global
        .offset:         48
        .size:           8
        .value_kind:     global_buffer
      - .actual_access:  read_only
        .address_space:  global
        .offset:         56
        .size:           8
        .value_kind:     global_buffer
      - .actual_access:  write_only
        .address_space:  global
        .offset:         64
        .size:           8
        .value_kind:     global_buffer
      - .actual_access:  write_only
        .address_space:  global
        .offset:         72
        .size:           8
        .value_kind:     global_buffer
    .group_segment_fixed_size: 53248
    .kernarg_segment_align: 8
    .kernarg_segment_size: 80
    .language:       OpenCL C
    .language_version:
      - 2
      - 0
    .max_flat_workgroup_size: 512
    .name:           _Z4k_l2PK15HIP_vector_typeIiLj4EES2_PKiPiS5_PKfPKDv8_DF16_S7_PDF16_SB_
    .private_segment_fixed_size: 0
    .sgpr_count:     34
    .sgpr_spill_count: 0
    .symbol:         _Z4k_l2PK15HIP_vector_typeIiLj4EES2_PKiPiS5_PKfPKDv8_DF16_S7_PDF16_SB_.kd
    .uniform_work_group_size: 1
    .uses_dynamic_stack: false
    .vgpr_count:     126
    .vgpr_spill_count: 0
    .wavefront_size: 64
